# static priority raise (s_setprio 3) for the 256 latency-critical partition workgroups of k_prep
# baseline (speedup 1.0000x reference)
.LBB0_24:
	s_andn2_b64 vcc, exec, s[4:5]
	s_mov_b32 s9, 1
	s_cbranch_vccnz .LBB0_135
	s_setprio 3
	s_and_b32 s10, s2, 7
	s_lshr_b32 s2, s2, 3
	s_lshl_b32 s10, s10, 5
	s_or_b32 s2, s2, s10
	s_load_dwordx2 s[6:7], s[0:1], 0x58
	s_load_dwordx2 s[4:5], s[0:1], 0x0
	s_load_dwordx4 s[28:31], s[0:1], 0x28
	v_lshlrev_b32_e32 v12, 2, v0
	s_mov_b32 s8, 0
	v_add_u32_e32 v1, 0x30e0, v12
	s_mov_b64 s[0:1], 0
	v_mov_b32_e32 v2, 0
	s_mov_b32 s10, s8
	s_branch .LBB0_27
